# grid barrier: non-leader workgroups poll the cross-XCD release word (TOPGEN) directly instead of waiting for their XCD leader's relay (XGEN)
# speedup vs baseline: 1.0155x; 1.0155x over previous
.LBB0_66:
	s_or_b64 exec, exec, s[6:7]
	v_cvt_f32_u32_e32 v5, v3
	s_waitcnt vmcnt(0)
	v_readfirstlane_b32 s4, v4
	v_sub_u32_e32 v4, 0, v3
	v_rcp_iflag_f32_e32 v5, v5
	v_add_u32_e32 v6, s4, v2
	v_mul_f32_e32 v5, 0x4f7ffffe, v5
	v_cvt_u32_f32_e32 v5, v5
	v_mul_lo_u32 v2, v4, v5
	v_mul_hi_u32 v2, v5, v2
	v_add_u32_e32 v2, v5, v2
	v_mul_hi_u32 v2, v6, v2
	v_mul_lo_u32 v4, v2, v3
	v_sub_u32_e32 v4, v6, v4
	v_add_u32_e32 v5, 1, v2
	v_cmp_ge_u32_e32 vcc, v4, v3
	s_nop 1
	v_cndmask_b32_e32 v2, v2, v5, vcc
	v_sub_u32_e32 v5, v4, v3
	v_cndmask_b32_e32 v4, v4, v5, vcc
	v_add_u32_e32 v5, 1, v2
	v_cmp_ge_u32_e32 vcc, v4, v3
	v_add_u32_e32 v4, 1, v6
	s_nop 0
	v_cndmask_b32_e32 v2, v2, v5, vcc
	v_mul_lo_u32 v5, v3, v2
	v_add_u32_e32 v3, v5, v3
	v_cmp_ne_u32_e32 vcc, v4, v3
	s_and_saveexec_b64 s[4:5], vcc
	s_xor_b64 s[4:5], exec, s[4:5]
	s_cbranch_execz .LBB0_80
	s_waitcnt lgkmcnt(0)
	v_readlane_b32 s10, v255, 4
	v_readlane_b32 s11, v255, 5
	s_add_u32 s10, s10, 0x3500
	s_addc_u32 s11, s11, 0
	v_mov_b32_e32 v1, 0
	global_load_dword v1, v1, s[10:11] sc1
	s_waitcnt vmcnt(0)
	v_cmp_eq_u32_e32 vcc, v1, v2
	s_and_saveexec_b64 s[6:7], vcc
	s_cbranch_execz .LBB0_79
	v_readlane_b32 s8, v255, 2
	v_readlane_b32 s9, v255, 3
	s_add_u32 s8, s8, 0x4200
	s_addc_u32 s9, s9, 0
	s_mov_b32 s22, 1
	s_mov_b64 s[12:13], 0
	v_mov_b32_e32 v1, 0
	s_branch .LBB0_70

.LBB0_403:
	s_or_b64 exec, exec, s[6:7]
	v_cvt_f32_u32_e32 v6, v4
	s_waitcnt vmcnt(0)
	v_readfirstlane_b32 s4, v5
	v_sub_u32_e32 v5, 0, v4
	v_rcp_iflag_f32_e32 v6, v6
	v_add_u32_e32 v7, s4, v3
	v_mul_f32_e32 v6, 0x4f7ffffe, v6
	v_cvt_u32_f32_e32 v6, v6
	v_mul_lo_u32 v3, v5, v6
	v_mul_hi_u32 v3, v6, v3
	v_add_u32_e32 v3, v6, v3
	v_mul_hi_u32 v3, v7, v3
	v_mul_lo_u32 v5, v3, v4
	v_sub_u32_e32 v5, v7, v5
	v_add_u32_e32 v6, 1, v3
	v_cmp_ge_u32_e32 vcc, v5, v4
	s_nop 1
	v_cndmask_b32_e32 v3, v3, v6, vcc
	v_sub_u32_e32 v6, v5, v4
	v_cndmask_b32_e32 v5, v5, v6, vcc
	v_add_u32_e32 v6, 1, v3
	v_cmp_ge_u32_e32 vcc, v5, v4
	v_add_u32_e32 v5, 1, v7
	s_nop 0
	v_cndmask_b32_e32 v3, v3, v6, vcc
	v_mul_lo_u32 v6, v4, v3
	v_add_u32_e32 v4, v6, v4
	v_cmp_ne_u32_e32 vcc, v5, v4
	s_and_saveexec_b64 s[4:5], vcc
	s_xor_b64 s[4:5], exec, s[4:5]
	s_cbranch_execz .LBB0_417
	s_waitcnt lgkmcnt(0)
	v_readlane_b32 s10, v255, 4
	v_readlane_b32 s11, v255, 5
	s_add_u32 s10, s10, 0x3500
	s_addc_u32 s11, s11, 0
	v_mov_b32_e32 v2, 0
	global_load_dword v2, v2, s[10:11] sc1
	s_waitcnt vmcnt(0)
	v_cmp_eq_u32_e32 vcc, v2, v3
	s_and_saveexec_b64 s[6:7], vcc
	s_cbranch_execz .LBB0_416
	v_readlane_b32 s8, v255, 2
	v_readlane_b32 s9, v255, 3
	s_add_u32 s8, s8, 0x4200
	s_addc_u32 s9, s9, 0
	s_mov_b32 s22, 1
	s_mov_b64 s[12:13], 0
	v_mov_b32_e32 v2, 0
	s_branch .LBB0_407

.LBB0_495:
	s_or_b64 exec, exec, s[6:7]
	v_cvt_f32_u32_e32 v6, v4
	s_waitcnt vmcnt(0)
	v_readfirstlane_b32 s4, v5
	v_sub_u32_e32 v5, 0, v4
	v_rcp_iflag_f32_e32 v6, v6
	v_add_u32_e32 v7, s4, v3
	v_mul_f32_e32 v6, 0x4f7ffffe, v6
	v_cvt_u32_f32_e32 v6, v6
	v_mul_lo_u32 v3, v5, v6
	v_mul_hi_u32 v3, v6, v3
	v_add_u32_e32 v3, v6, v3
	v_mul_hi_u32 v3, v7, v3
	v_mul_lo_u32 v5, v3, v4
	v_sub_u32_e32 v5, v7, v5
	v_add_u32_e32 v6, 1, v3
	v_cmp_ge_u32_e32 vcc, v5, v4
	s_nop 1
	v_cndmask_b32_e32 v3, v3, v6, vcc
	v_sub_u32_e32 v6, v5, v4
	v_cndmask_b32_e32 v5, v5, v6, vcc
	v_add_u32_e32 v6, 1, v3
	v_cmp_ge_u32_e32 vcc, v5, v4
	v_add_u32_e32 v5, 1, v7
	s_nop 0
	v_cndmask_b32_e32 v3, v3, v6, vcc
	v_mul_lo_u32 v6, v4, v3
	v_add_u32_e32 v4, v6, v4
	v_cmp_ne_u32_e32 vcc, v5, v4
	s_and_saveexec_b64 s[4:5], vcc
	s_xor_b64 s[4:5], exec, s[4:5]
	s_cbranch_execz .LBB0_509
	s_waitcnt lgkmcnt(0)
	v_readlane_b32 s12, v255, 4
	v_readlane_b32 s13, v255, 5
	s_add_u32 s12, s12, 0x3500
	s_addc_u32 s13, s13, 0
	v_mov_b32_e32 v2, 0
	global_load_dword v2, v2, s[12:13] sc1
	s_waitcnt vmcnt(0)
	v_cmp_eq_u32_e32 vcc, v2, v3
	s_and_saveexec_b64 s[6:7], vcc
	s_cbranch_execz .LBB0_508
	v_readlane_b32 s10, v255, 2
	v_readlane_b32 s11, v255, 3
	s_add_u32 s10, s10, 0x4200
	s_addc_u32 s11, s11, 0
	s_mov_b32 s24, 1
	s_mov_b64 s[14:15], 0
	v_mov_b32_e32 v2, 0
	s_branch .LBB0_499

.LBB0_673:
	s_or_b64 exec, exec, s[6:7]
	v_cvt_f32_u32_e32 v5, v3
	s_waitcnt vmcnt(0)
	v_readfirstlane_b32 s4, v4
	v_sub_u32_e32 v4, 0, v3
	v_rcp_iflag_f32_e32 v5, v5
	v_add_u32_e32 v6, s4, v2
	v_mul_f32_e32 v5, 0x4f7ffffe, v5
	v_cvt_u32_f32_e32 v5, v5
	v_mul_lo_u32 v2, v4, v5
	v_mul_hi_u32 v2, v5, v2
	v_add_u32_e32 v2, v5, v2
	v_mul_hi_u32 v2, v6, v2
	v_mul_lo_u32 v4, v2, v3
	v_sub_u32_e32 v4, v6, v4
	v_add_u32_e32 v5, 1, v2
	v_cmp_ge_u32_e32 vcc, v4, v3
	s_nop 1
	v_cndmask_b32_e32 v2, v2, v5, vcc
	v_sub_u32_e32 v5, v4, v3
	v_cndmask_b32_e32 v4, v4, v5, vcc
	v_add_u32_e32 v5, 1, v2
	v_cmp_ge_u32_e32 vcc, v4, v3
	v_add_u32_e32 v4, 1, v6
	s_nop 0
	v_cndmask_b32_e32 v2, v2, v5, vcc
	v_mul_lo_u32 v5, v3, v2
	v_add_u32_e32 v3, v5, v3
	v_cmp_ne_u32_e32 vcc, v4, v3
	s_and_saveexec_b64 s[4:5], vcc
	s_xor_b64 s[4:5], exec, s[4:5]
	s_cbranch_execz .LBB0_687
	s_waitcnt lgkmcnt(0)
	v_readlane_b32 s12, v255, 4
	v_readlane_b32 s13, v255, 5
	s_add_u32 s12, s12, 0x3500
	s_addc_u32 s13, s13, 0
	v_mov_b32_e32 v1, 0
	global_load_dword v1, v1, s[12:13] sc1
	s_waitcnt vmcnt(0)
	v_cmp_eq_u32_e32 vcc, v1, v2
	s_and_saveexec_b64 s[6:7], vcc
	s_cbranch_execz .LBB0_686
	v_readlane_b32 s10, v255, 2
	v_readlane_b32 s11, v255, 3
	s_add_u32 s10, s10, 0x4200
	s_addc_u32 s11, s11, 0
	s_mov_b32 s24, 1
	s_mov_b64 s[14:15], 0
	v_mov_b32_e32 v1, 0
	s_branch .LBB0_677

.LBB0_749:
	s_or_b64 exec, exec, s[6:7]
	v_cvt_f32_u32_e32 v4, v2
	s_waitcnt vmcnt(0)
	v_readfirstlane_b32 s4, v3
	v_sub_u32_e32 v3, 0, v2
	v_rcp_iflag_f32_e32 v4, v4
	v_add_u32_e32 v5, s4, v1
	v_mul_f32_e32 v4, 0x4f7ffffe, v4
	v_cvt_u32_f32_e32 v4, v4
	v_mul_lo_u32 v1, v3, v4
	v_mul_hi_u32 v1, v4, v1
	v_add_u32_e32 v1, v4, v1
	v_mul_hi_u32 v1, v5, v1
	v_mul_lo_u32 v3, v1, v2
	v_sub_u32_e32 v3, v5, v3
	v_add_u32_e32 v4, 1, v1
	v_cmp_ge_u32_e32 vcc, v3, v2
	s_nop 1
	v_cndmask_b32_e32 v1, v1, v4, vcc
	v_sub_u32_e32 v4, v3, v2
	v_cndmask_b32_e32 v3, v3, v4, vcc
	v_add_u32_e32 v4, 1, v1
	v_cmp_ge_u32_e32 vcc, v3, v2
	v_add_u32_e32 v3, 1, v5
	s_nop 0
	v_cndmask_b32_e32 v1, v1, v4, vcc
	v_mul_lo_u32 v4, v2, v1
	v_add_u32_e32 v2, v4, v2
	v_cmp_ne_u32_e32 vcc, v3, v2
	s_and_saveexec_b64 s[4:5], vcc
	s_xor_b64 s[4:5], exec, s[4:5]
	s_cbranch_execz .LBB0_763
	s_waitcnt lgkmcnt(0)
	v_readlane_b32 s10, v255, 4
	v_readlane_b32 s11, v255, 5
	s_add_u32 s10, s10, 0x3500
	s_addc_u32 s11, s11, 0
	v_mov_b32_e32 v0, 0
	global_load_dword v0, v0, s[10:11] sc1
	s_waitcnt vmcnt(0)
	v_cmp_eq_u32_e32 vcc, v0, v1
	s_and_saveexec_b64 s[6:7], vcc
	s_cbranch_execz .LBB0_762
	v_readlane_b32 s8, v255, 2
	v_readlane_b32 s9, v255, 3
	s_add_u32 s8, s8, 0x4200
	s_addc_u32 s9, s9, 0
	s_mov_b32 s22, 1
	s_mov_b64 s[12:13], 0
	v_mov_b32_e32 v0, 0
	s_branch .LBB0_753

.LBB0_835:
	s_or_b64 exec, exec, s[8:9]
	v_cvt_f32_u32_e32 v4, v2
	s_waitcnt vmcnt(0)
	v_readfirstlane_b32 s3, v3
	v_sub_u32_e32 v3, 0, v2
	v_rcp_iflag_f32_e32 v4, v4
	v_add_u32_e32 v5, s3, v1
	v_mul_f32_e32 v4, 0x4f7ffffe, v4
	v_cvt_u32_f32_e32 v4, v4
	v_mul_lo_u32 v1, v3, v4
	v_mul_hi_u32 v1, v4, v1
	v_add_u32_e32 v1, v4, v1
	v_mul_hi_u32 v1, v5, v1
	v_mul_lo_u32 v3, v1, v2
	v_sub_u32_e32 v3, v5, v3
	v_add_u32_e32 v4, 1, v1
	v_cmp_ge_u32_e32 vcc, v3, v2
	s_nop 1
	v_cndmask_b32_e32 v1, v1, v4, vcc
	v_sub_u32_e32 v4, v3, v2
	v_cndmask_b32_e32 v3, v3, v4, vcc
	v_add_u32_e32 v4, 1, v1
	v_cmp_ge_u32_e32 vcc, v3, v2
	v_add_u32_e32 v3, 1, v5
	s_nop 0
	v_cndmask_b32_e32 v1, v1, v4, vcc
	v_mul_lo_u32 v4, v2, v1
	v_add_u32_e32 v2, v4, v2
	v_cmp_ne_u32_e32 vcc, v3, v2
	s_and_saveexec_b64 s[6:7], vcc
	s_xor_b64 s[6:7], exec, s[6:7]
	s_cbranch_execz .LBB0_849
	s_waitcnt lgkmcnt(0)
	v_readlane_b32 s12, v255, 4
	v_readlane_b32 s13, v255, 5
	s_add_u32 s12, s12, 0x3500
	s_addc_u32 s13, s13, 0
	v_mov_b32_e32 v0, 0
	global_load_dword v0, v0, s[12:13] sc1
	s_waitcnt vmcnt(0)
	v_cmp_eq_u32_e32 vcc, v0, v1
	s_and_saveexec_b64 s[8:9], vcc
	s_cbranch_execz .LBB0_848
	v_readlane_b32 s10, v255, 2
	v_readlane_b32 s11, v255, 3
	s_add_u32 s10, s10, 0x4200
	s_addc_u32 s11, s11, 0
	s_mov_b32 s3, 1
	s_mov_b64 s[14:15], 0
	v_mov_b32_e32 v0, 0
	s_branch .LBB0_839
